# attention step head trimmed: no-op lgkmcnt ladder inside the bias adds removed, LDS-DMA issue blocks write m0 directly
# speedup vs baseline: 1.0015x; 1.0015x over previous
.LBB0_726:
	v_add_u32_e32 v164, s18, v239
	s_add_i32 m0, s38, s30
	s_nop 0
	global_load_lds_dwordx4 v244, s[98:99]
	s_add_i32 m0, s22, s31
	s_nop 0
	global_load_lds_dwordx4 v245, s[98:99]
	s_add_u32 s98, s98, 0x20000
	s_addc_u32 s99, s99, 0
	ds_read_b64_tr_b16 v[190:191], v164 offset:24576
	ds_read_b64_tr_b16 v[192:193], v164 offset:25088
	s_waitcnt lgkmcnt(2)
	v_mfma_f32_32x32x16_bf16 v[48:63], v[158:161], v[110:113], v[48:63]
	v_add_f32_e32 v114, v80, v81
	v_add_f32_e32 v114, v82, v114
	v_add_f32_e32 v114, v83, v114
	v_add_f32_e32 v114, v84, v114
	v_add_f32_e32 v114, v85, v114
	v_cvt_pk_bf16_f32 v126, v80, v81
	v_cvt_pk_bf16_f32 v127, v82, v83
	ds_read_b64_tr_b16 v[186:187], v164 offset:28672
	ds_read_b64_tr_b16 v[188:189], v164 offset:29184
	v_mfma_f32_32x32x16_bf16 v[32:47], v[146:149], v[110:113], v[32:47]
	v_add_f32_e32 v80, v86, v114
	v_add_f32_e32 v80, v87, v80
	v_add_f32_e32 v80, v88, v80
	v_add_f32_e32 v80, v89, v80
	v_cvt_pk_bf16_f32 v128, v84, v85
	v_cvt_pk_bf16_f32 v129, v86, v87
	ds_read_b64_tr_b16 v[182:183], v164 offset:25600
	ds_read_b64_tr_b16 v[184:185], v164 offset:26112
	v_mfma_f32_32x32x16_bf16 v[48:63], v[154:157], v[106:109], v[48:63]
	v_add_f32_e32 v80, v90, v80
	v_add_f32_e32 v80, v91, v80
	v_add_f32_e32 v80, v92, v80
	v_add_f32_e32 v80, v93, v80
	v_cvt_pk_bf16_f32 v122, v88, v89
	v_cvt_pk_bf16_f32 v123, v90, v91
	ds_read_b64_tr_b16 v[178:179], v164 offset:29696
	ds_read_b64_tr_b16 v[180:181], v164 offset:30208
	v_mfma_f32_32x32x16_bf16 v[32:47], v[142:145], v[106:109], v[32:47]
	v_add_f32_e32 v80, v94, v80
	v_add_f32_e32 v80, v95, v80
	v_add_f32_e32 v80, v64, v80
	v_add_f32_e32 v80, v65, v80
	v_cvt_pk_bf16_f32 v124, v92, v93
	v_cvt_pk_bf16_f32 v125, v94, v95
	ds_read_b64_tr_b16 v[166:167], v164 offset:26624
	ds_read_b64_tr_b16 v[168:169], v164 offset:27136
	v_mfma_f32_32x32x16_bf16 v[48:63], v[150:153], v[102:105], v[48:63]
	v_add_f32_e32 v80, v66, v80
	v_add_f32_e32 v80, v67, v80
	v_add_f32_e32 v80, v68, v80
	v_add_f32_e32 v80, v69, v80
	v_cvt_pk_bf16_f32 v118, v64, v65
	v_cvt_pk_bf16_f32 v119, v66, v67
	ds_read_b64_tr_b16 v[174:175], v164 offset:30720
	ds_read_b64_tr_b16 v[176:177], v164 offset:31232
	v_mfma_f32_32x32x16_bf16 v[32:47], v[138:141], v[102:105], v[32:47]
	v_add_f32_e32 v64, v70, v80
	v_add_f32_e32 v64, v71, v64
	v_add_f32_e32 v64, v72, v64
	v_add_f32_e32 v64, v73, v64
	v_cvt_pk_bf16_f32 v120, v68, v69
	v_cvt_pk_bf16_f32 v121, v70, v71
	ds_read_b64_tr_b16 v[170:171], v164 offset:27648
	ds_read_b64_tr_b16 v[172:173], v164 offset:28160
	v_mfma_f32_32x32x16_bf16 v[48:63], v[134:137], v[98:101], v[48:63]
	v_add_f32_e32 v64, v74, v64
	v_add_f32_e32 v64, v75, v64
	v_add_f32_e32 v64, v76, v64
	v_add_f32_e32 v64, v77, v64
	v_cvt_pk_bf16_f32 v114, v72, v73
	v_cvt_pk_bf16_f32 v115, v74, v75
	ds_read_b64_tr_b16 v[162:163], v164 offset:31744
	ds_read_b64_tr_b16 v[164:165], v164 offset:32256
	v_mfma_f32_32x32x16_bf16 v[32:47], v[130:133], v[98:101], v[32:47]
	v_add_f32_e32 v64, v78, v64
	v_add_f32_e32 v64, v79, v64
	v_add_f32_e32 v224, v240, v64
	v_cvt_pk_bf16_f32 v116, v76, v77
	v_cvt_pk_bf16_f32 v117, v78, v79
	s_waitcnt lgkmcnt(14)
	ds_read_b128 v[64:67], v205
	ds_read_b128 v[68:71], v205 offset:32
	ds_read_b128 v[82:85], v205 offset:128
	ds_read_b128 v[86:89], v205 offset:160
	ds_read_b128 v[72:75], v205 offset:64
	ds_read_b128 v[76:79], v205 offset:96
	ds_read_b128 v[90:93], v205 offset:192
	ds_read_b128 v[138:141], v205 offset:224
	v_max_f32_e32 v80, v48, v49
	v_max3_f32 v81, v50, v51, v33
	v_max3_f32 v80, v80, v32, v34
	v_max3_f32 v80, v80, v35, v52
	v_max3_f32 v81, v81, v54, v55
	v_max3_f32 v80, v80, v53, v36
	v_max3_f32 v81, v81, v38, v39
	v_max3_f32 v80, v80, v37, v56
	v_max3_f32 v81, v81, v58, v59
	v_max3_f32 v80, v80, v57, v40
	v_max3_f32 v81, v81, v42, v43
	v_max3_f32 v80, v80, v41, v60
	v_max3_f32 v81, v81, v62, v63
	v_max3_f32 v80, v80, v61, v44
	v_max3_f32 v81, v81, v46, v47
	v_max3_f32 v80, v80, v45, v81
	v_mov_b32_e32 v81, v80
	s_nop 1
	v_permlane32_swap_b32_e32 v80, v81
	v_max_f32_e32 v80, v80, v81
	v_cmp_lt_f32_e32 vcc, s51, v80
	s_cmp_lg_u64 vcc, 0
	s_cselect_b64 s[18:19], -1, 0
	s_cbranch_vccnz .LBB0_734

.LBB0_729:
	v_pk_add_f32 v[80:81], v[64:65], v[202:203] op_sel_hi:[1,0] neg_lo:[0,1] neg_hi:[0,1]
	v_pk_add_f32 v[64:65], v[82:83], v[202:203] op_sel_hi:[1,0] neg_lo:[0,1] neg_hi:[0,1]
	v_pk_add_f32 v[82:83], v[66:67], v[202:203] op_sel_hi:[1,0] neg_lo:[0,1] neg_hi:[0,1]
	v_pk_add_f32 v[66:67], v[84:85], v[202:203] op_sel_hi:[1,0] neg_lo:[0,1] neg_hi:[0,1]
	v_pk_add_f32 v[84:85], v[68:69], v[202:203] op_sel_hi:[1,0] neg_lo:[0,1] neg_hi:[0,1]
	v_pk_add_f32 v[68:69], v[86:87], v[202:203] op_sel_hi:[1,0] neg_lo:[0,1] neg_hi:[0,1]
	v_pk_add_f32 v[86:87], v[70:71], v[202:203] op_sel_hi:[1,0] neg_lo:[0,1] neg_hi:[0,1]
	v_pk_add_f32 v[70:71], v[88:89], v[202:203] op_sel_hi:[1,0] neg_lo:[0,1] neg_hi:[0,1]
	v_pk_add_f32 v[88:89], v[72:73], v[202:203] op_sel_hi:[1,0] neg_lo:[0,1] neg_hi:[0,1]
	v_pk_add_f32 v[72:73], v[90:91], v[202:203] op_sel_hi:[1,0] neg_lo:[0,1] neg_hi:[0,1]
	v_pk_add_f32 v[90:91], v[74:75], v[202:203] op_sel_hi:[1,0] neg_lo:[0,1] neg_hi:[0,1]
	v_pk_add_f32 v[74:75], v[92:93], v[202:203] op_sel_hi:[1,0] neg_lo:[0,1] neg_hi:[0,1]
	v_pk_add_f32 v[92:93], v[76:77], v[202:203] op_sel_hi:[1,0] neg_lo:[0,1] neg_hi:[0,1]
	v_pk_add_f32 v[76:77], v[138:139], v[202:203] op_sel_hi:[1,0] neg_lo:[0,1] neg_hi:[0,1]
	v_pk_add_f32 v[94:95], v[78:79], v[202:203] op_sel_hi:[1,0] neg_lo:[0,1] neg_hi:[0,1]
	v_pk_add_f32 v[78:79], v[140:141], v[202:203] op_sel_hi:[1,0] neg_lo:[0,1] neg_hi:[0,1]
	s_add_i32 s18, s22, 0x2000
	v_add_u32_e32 v162, s38, v239
	s_cmpk_lg_i32 s22, 0x4000
	s_cselect_b32 s38, s18, 0
	s_add_i32 m0, s22, s30
	s_nop 0
	global_load_lds_dwordx4 v244, s[98:99]
	s_add_i32 m0, s38, s31
	s_nop 0
	global_load_lds_dwordx4 v245, s[98:99]
	s_add_u32 s98, s98, 0x20000
	s_addc_u32 s99, s99, 0
	ds_read_b64_tr_b16 v[194:195], v162 offset:24576
	ds_read_b64_tr_b16 v[196:197], v162 offset:25088
	s_waitcnt lgkmcnt(2)
	v_mfma_f32_32x32x16_bf16 v[80:95], v[134:137], v[110:113], v[80:95]
	v_add_f32_e32 v114, v48, v49
	v_add_f32_e32 v114, v50, v114
	v_add_f32_e32 v114, v51, v114
	v_add_f32_e32 v114, v52, v114
	v_add_f32_e32 v114, v53, v114
	v_cvt_pk_bf16_f32 v126, v48, v49
	v_cvt_pk_bf16_f32 v127, v50, v51
	ds_read_b64_tr_b16 v[190:191], v162 offset:28672
	ds_read_b64_tr_b16 v[192:193], v162 offset:29184
	v_mfma_f32_32x32x16_bf16 v[64:79], v[130:133], v[110:113], v[64:79]
	v_add_f32_e32 v48, v54, v114
	v_add_f32_e32 v48, v55, v48
	v_add_f32_e32 v48, v56, v48
	v_add_f32_e32 v48, v57, v48
	v_cvt_pk_bf16_f32 v128, v52, v53
	v_cvt_pk_bf16_f32 v129, v54, v55
	ds_read_b64_tr_b16 v[186:187], v162 offset:25600
	ds_read_b64_tr_b16 v[188:189], v162 offset:26112
	v_mfma_f32_32x32x16_bf16 v[80:95], v[146:149], v[106:109], v[80:95]
	v_add_f32_e32 v48, v58, v48
	v_add_f32_e32 v48, v59, v48
	v_add_f32_e32 v48, v60, v48
	v_add_f32_e32 v48, v61, v48
	v_cvt_pk_bf16_f32 v122, v56, v57
	v_cvt_pk_bf16_f32 v123, v58, v59
	ds_read_b64_tr_b16 v[138:139], v162 offset:29696
	ds_read_b64_tr_b16 v[140:141], v162 offset:30208
	v_mfma_f32_32x32x16_bf16 v[64:79], v[142:145], v[106:109], v[64:79]
	v_add_f32_e32 v48, v62, v48
	v_add_f32_e32 v48, v63, v48
	v_add_f32_e32 v48, v32, v48
	v_add_f32_e32 v48, v33, v48
	v_cvt_pk_bf16_f32 v124, v60, v61
	v_cvt_pk_bf16_f32 v125, v62, v63
	ds_read_b64_tr_b16 v[182:183], v162 offset:26624
	ds_read_b64_tr_b16 v[184:185], v162 offset:27136
	v_mfma_f32_32x32x16_bf16 v[80:95], v[158:161], v[102:105], v[80:95]
	v_add_f32_e32 v48, v34, v48
	v_add_f32_e32 v48, v35, v48
	v_add_f32_e32 v48, v36, v48
	v_add_f32_e32 v48, v37, v48
	v_cvt_pk_bf16_f32 v118, v32, v33
	v_cvt_pk_bf16_f32 v119, v34, v35
	ds_read_b64_tr_b16 v[178:179], v162 offset:30720
	ds_read_b64_tr_b16 v[180:181], v162 offset:31232
	v_mfma_f32_32x32x16_bf16 v[64:79], v[154:157], v[102:105], v[64:79]
	v_add_f32_e32 v32, v38, v48
	v_add_f32_e32 v32, v39, v32
	v_add_f32_e32 v32, v40, v32
	v_add_f32_e32 v32, v41, v32
	v_cvt_pk_bf16_f32 v120, v36, v37
	v_cvt_pk_bf16_f32 v121, v38, v39
	ds_read_b64_tr_b16 v[174:175], v162 offset:27648
	ds_read_b64_tr_b16 v[176:177], v162 offset:28160
	v_mfma_f32_32x32x16_bf16 v[80:95], v[166:169], v[98:101], v[80:95]
	v_add_f32_e32 v32, v42, v32
	v_add_f32_e32 v32, v43, v32
	v_add_f32_e32 v32, v44, v32
	v_add_f32_e32 v32, v45, v32
	v_cvt_pk_bf16_f32 v114, v40, v41
	v_cvt_pk_bf16_f32 v115, v42, v43
	ds_read_b64_tr_b16 v[170:171], v162 offset:31744
	ds_read_b64_tr_b16 v[172:173], v162 offset:32256
	v_mfma_f32_32x32x16_bf16 v[64:79], v[150:153], v[98:101], v[64:79]
	v_add_f32_e32 v32, v46, v32
	v_add_f32_e32 v32, v47, v32
	v_add_f32_e32 v240, v224, v32
	v_cvt_pk_bf16_f32 v116, v44, v45
	v_cvt_pk_bf16_f32 v117, v46, v47
	s_waitcnt lgkmcnt(14)
	ds_read_b128 v[32:35], v205 offset:256
	ds_read_b128 v[36:39], v205 offset:288
	ds_read_b128 v[50:53], v205 offset:384
	ds_read_b128 v[54:57], v205 offset:416
	ds_read_b128 v[40:43], v205 offset:320
	ds_read_b128 v[44:47], v205 offset:352
	ds_read_b128 v[58:61], v205 offset:448
	ds_read_b128 v[162:165], v205 offset:480
	v_max_f32_e32 v48, v80, v81
	v_max3_f32 v49, v82, v83, v65
	v_max3_f32 v48, v48, v64, v66
	v_max3_f32 v48, v48, v67, v84
	v_max3_f32 v49, v49, v86, v87
	v_max3_f32 v48, v48, v85, v68
	v_max3_f32 v49, v49, v70, v71
	v_max3_f32 v48, v48, v69, v88
	v_max3_f32 v49, v49, v90, v91
	v_max3_f32 v48, v48, v89, v72
	v_max3_f32 v49, v49, v74, v75
	v_max3_f32 v48, v48, v73, v92
	v_max3_f32 v49, v49, v94, v95
	v_max3_f32 v48, v48, v93, v76
	v_max3_f32 v49, v49, v78, v79
	v_max3_f32 v48, v48, v77, v49
	v_mov_b32_e32 v49, v48
	s_nop 1
	v_permlane32_swap_b32_e32 v48, v49
	v_max_f32_e32 v48, v48, v49
	v_cmp_lt_f32_e32 vcc, s51, v48
	s_cmp_lg_u64 vcc, 0
	s_cselect_b64 s[18:19], -1, 0
	s_cbranch_vccnz .LBB0_737

.LBB0_732:
	s_add_i32 s18, s38, 0x2000
	s_cmpk_lg_i32 s38, 0x4000
	s_cselect_b32 s46, s18, 0
	s_add_i32 s18, s23, 2
	s_mov_b64 s[20:21], 0x40000
	v_pk_add_f32 v[48:49], v[32:33], v[202:203] op_sel_hi:[1,0] neg_lo:[0,1] neg_hi:[0,1]
	v_pk_add_f32 v[32:33], v[50:51], v[202:203] op_sel_hi:[1,0] neg_lo:[0,1] neg_hi:[0,1]
	v_pk_add_f32 v[50:51], v[34:35], v[202:203] op_sel_hi:[1,0] neg_lo:[0,1] neg_hi:[0,1]
	v_pk_add_f32 v[34:35], v[52:53], v[202:203] op_sel_hi:[1,0] neg_lo:[0,1] neg_hi:[0,1]
	v_pk_add_f32 v[52:53], v[36:37], v[202:203] op_sel_hi:[1,0] neg_lo:[0,1] neg_hi:[0,1]
	v_pk_add_f32 v[36:37], v[54:55], v[202:203] op_sel_hi:[1,0] neg_lo:[0,1] neg_hi:[0,1]
	v_pk_add_f32 v[54:55], v[38:39], v[202:203] op_sel_hi:[1,0] neg_lo:[0,1] neg_hi:[0,1]
	v_pk_add_f32 v[38:39], v[56:57], v[202:203] op_sel_hi:[1,0] neg_lo:[0,1] neg_hi:[0,1]
	v_pk_add_f32 v[56:57], v[40:41], v[202:203] op_sel_hi:[1,0] neg_lo:[0,1] neg_hi:[0,1]
	v_pk_add_f32 v[40:41], v[58:59], v[202:203] op_sel_hi:[1,0] neg_lo:[0,1] neg_hi:[0,1]
	v_pk_add_f32 v[58:59], v[42:43], v[202:203] op_sel_hi:[1,0] neg_lo:[0,1] neg_hi:[0,1]
	v_pk_add_f32 v[42:43], v[60:61], v[202:203] op_sel_hi:[1,0] neg_lo:[0,1] neg_hi:[0,1]
	v_pk_add_f32 v[60:61], v[44:45], v[202:203] op_sel_hi:[1,0] neg_lo:[0,1] neg_hi:[0,1]
	v_pk_add_f32 v[44:45], v[162:163], v[202:203] op_sel_hi:[1,0] neg_lo:[0,1] neg_hi:[0,1]
	v_pk_add_f32 v[62:63], v[46:47], v[202:203] op_sel_hi:[1,0] neg_lo:[0,1] neg_hi:[0,1]
	v_pk_add_f32 v[46:47], v[164:165], v[202:203] op_sel_hi:[1,0] neg_lo:[0,1] neg_hi:[0,1]
	v_lshl_add_u64 v[206:207], v[206:207], 0, s[20:21]
	s_mov_b64 s[62:63], 0x40000
	v_lshl_add_u64 v[208:209], v[208:209], 0, s[20:21]
	s_cmp_ge_u32 s18, s39
	v_add_u32_e32 v205, 0x200, v205
	s_cbranch_scc1 .LBB0_749
	s_mov_b32 s23, s18
	s_mov_b32 s18, s22
	s_mov_b32 s22, s46
	s_branch .LBB0_726
